# adds: router weight hi/lo copies stored fragment-major in the workspace (each LN1 weight-fragment load is one contiguous 1 KB instead of 16 rows x 64 B)
# speedup vs baseline: 1.0247x; 1.0041x over previous
; __device__ __forceinline__ unsigned f2bf(float f) { return pk2(f, 0.f); }
; __device__ __forceinline__ void phase_prologue_a(Frame& F0, const Args& A) {
;     ...
;     for (int i = gt; i < DEPTH * NEXP * D; i += NGT) { const int l = i >> 16, e = (i >> 10) & 63, k = i & 1023;
;         const float v = A.in[I_WR + F.z][((size_t)l * D + k) * NEXP + e]; const unsigned h = f2bf(v); const float lo = v - bf2f(h);
;         ((bf16*)(F.ws + WS_RTHI))[i] = (bf16)h; ((bf16*)(F.ws + WS_RTLO))[i] = (bf16)f2bf(lo); }
.LBB0_32:
	v_and_b32_e32 v18, 0xffff, v10
	v_and_b32_e32 v19, 7, v10
	v_bfe_u32 v20, v10, 10, 4
	v_lshl_or_b32 v19, v20, 3, v19
	v_bfe_u32 v20, v10, 3, 2
	v_lshl_or_b32 v19, v20, 7, v19
	v_bfe_u32 v20, v10, 5, 2
	v_lshl_or_b32 v19, v20, 9, v19
	v_bfe_u32 v20, v10, 14, 2
	v_lshl_or_b32 v19, v20, 11, v19
	v_bfe_u32 v20, v10, 7, 3
	v_lshl_or_b32 v19, v20, 13, v19
	v_sub_u32_e32 v16, v19, v18
	v_lshlrev_b32_e32 v16, 1, v16
	v_ashrrev_i32_e32 v17, 31, v16
	v_ashrrev_i32_e32 v12, 16, v10
	v_ashrrev_i32_e32 v13, 31, v12
	v_and_b32_e32 v6, 0xffc0, v9
	v_lshlrev_b64 v[12:13], 18, v[12:13]
	v_lshrrev_b32_e32 v11, 8, v10
	v_lshlrev_b32_e32 v6, 2, v6
	s_waitcnt lgkmcnt(0)
	v_lshl_add_u64 v[12:13], s[10:11], 0, v[12:13]
	v_lshl_add_u64 v[12:13], v[12:13], 0, v[6:7]
	v_and_b32_e32 v6, 0xfc, v11
	v_lshl_add_u64 v[12:13], v[12:13], 0, v[6:7]
	global_load_dword v6, v[12:13], off
	v_add_co_u32_e32 v12, vcc, 0x80000, v4
	v_add_u32_e32 v10, s0, v10
	s_nop 0
	v_addc_co_u32_e32 v13, vcc, 0, v5, vcc
	v_cmp_lt_i32_e32 vcc, s14, v10
	v_add_u32_e32 v9, s1, v9
	s_or_b64 s[12:13], vcc, s[12:13]
	s_waitcnt vmcnt(0)
	v_cvt_pk_bf16_f32 v11, v6, 0
	v_lshlrev_b32_e32 v14, 16, v11
	v_sub_f32_e32 v6, v6, v14
	v_lshl_add_u64 v[18:19], v[4:5], 0, v[16:17]
	v_lshl_add_u64 v[20:21], v[12:13], 0, v[16:17]
	global_store_short v[18:19], v11, off
	v_lshl_add_u64 v[4:5], v[4:5], 0, s[8:9]
	v_cvt_pk_bf16_f32 v6, v6, s0
	global_store_short v[20:21], v6, off
	s_andn2_b64 exec, exec, s[12:13]
	s_cbranch_execnz .LBB0_32
	s_or_b64 exec, exec, s[12:13]
	s_mov_b64 s[10:11], 0x500000
	v_lshl_add_u64 v[2:3], v[2:3], 0, s[10:11]
	s_mov_b64 s[10:11], 0
	v_mov_b32_e32 v6, 0xe0
	v_mov_b32_e32 v7, 0xd0
	v_mov_b32_e32 v5, 0
	s_mov_b32 s12, 0x3ffff
	v_mov_b32_e32 v9, v0

; __device__ __forceinline__ void phase_ln1(Frame& F0, const Args& A, int l, bool v_from_h) {
;     ...
;     bf16x8 wh[4][4], wl[4][4];
;     const unsigned wloff = (unsigned)(fr * D + fq * 8) * 2u;
;     const char* rhb[4]; const char* rlb[4];
; #pragma unroll
;     for (int eg = 0; eg < 4; ++eg) { rhb[eg] = (const char*)(RH + wave * 128) + eg * 16 * D * 2; rlb[eg] = (const char*)(RL + wave * 128) + eg * 16 * D * 2; }
;     ...
;     LN1_GLDK(0); LN1_GLDK(1);
;     int pend_r[2] = {-1, -1}; float pend_w[2] = {0.f, 0.f};
;     ...
;     const float brl = brt[lane];
.LBB0_1283:
	s_lshl_b64 s[0:1], s[50:51], 2
	s_add_u32 s2, s24, s0
	s_addc_u32 s3, s25, s1
	v_readlane_b32 s0, v254, 44
	v_readlane_b32 s1, v254, 45
	s_lshl_b64 s[0:1], s[0:1], 17
	s_add_u32 s17, s22, s0
	s_addc_u32 s18, s23, s1
	s_add_u32 s6, s22, 0x600000
	s_addc_u32 s7, s23, 0
	s_add_u32 s8, s22, 0x800000
	s_addc_u32 s9, s23, 0
	s_lshl_b32 s0, s4, 7
	s_ashr_i32 s1, s0, 31
	s_lshl_b64 s[12:13], s[0:1], 7
	s_add_u32 s1, s17, s12
	s_addc_u32 s12, s18, s13
	s_add_u32 s20, s1, 0x400000
	s_addc_u32 s21, s12, 0
	s_add_u32 s24, s1, 0x480000
	s_addc_u32 s25, s12, 0
	s_add_u32 s26, s1, 0x401000
	s_addc_u32 s27, s12, 0
	s_add_u32 s42, s1, 0x481000
	v_and_b32_e32 v65, 15, v128
	v_and_b32_e32 v64, -16, v128
	s_addc_u32 s43, s12, 0
	s_nop 4
	s_add_u32 s50, s1, 0x402000
	v_lshlrev_b32_e32 v219, 4, v128
	global_load_dwordx4 v[0:3], v219, s[20:21] offset:0
	s_addc_u32 s51, s12, 0
	s_waitcnt vmcnt(0)
	global_load_dwordx4 v[4:7], v219, s[24:25] offset:0
	s_add_u32 s62, s1, 0x482000
	global_load_dwordx4 v[8:11], v219, s[26:27] offset:0
	s_addc_u32 s63, s12, 0
	global_load_dwordx4 v[12:15], v219, s[42:43] offset:0
	s_add_u32 s68, s1, 0x403000
	global_load_dwordx4 v[16:19], v219, s[50:51] offset:0
	s_addc_u32 s69, s12, 0
	global_load_dwordx4 v[20:23], v219, s[62:63] offset:0
	s_add_u32 s74, s1, 0x483000
	global_load_dwordx4 v[24:27], v219, s[68:69] offset:0
	s_addc_u32 s75, s12, 0
	global_load_dwordx4 v[28:31], v219, s[74:75] offset:0
	s_nop 4
	global_load_dwordx4 v[32:35], v219, s[20:21] offset:1024
	global_load_dwordx4 v[36:39], v219, s[24:25] offset:1024
	global_load_dwordx4 v[40:43], v219, s[26:27] offset:1024
	global_load_dwordx4 v[44:47], v219, s[42:43] offset:1024
	global_load_dwordx4 v[48:51], v219, s[50:51] offset:1024
	global_load_dwordx4 v[52:55], v219, s[62:63] offset:1024
	global_load_dwordx4 v[56:59], v219, s[68:69] offset:1024
	v_ashrrev_i32_e32 v129, 31, v128
	global_load_dwordx4 v[60:63], v219, s[74:75] offset:1024
	v_lshl_add_u64 v[66:67], v[128:129], 2, s[2:3]
	global_load_dword v148, v[66:67], off
	s_waitcnt lgkmcnt(0)
	s_barrier
	s_andn2_b64 vcc, exec, s[46:47]
	s_cbranch_vccnz .LBB0_1302
	v_lshrrev_b32_e32 v66, 1, v128
	v_and_b32_e32 v66, 0x7ffffff8, v66
	v_mul_u32_u24_e32 v67, 0x408, v65
	s_lshl_b32 s1, s4, 12
	v_readlane_b32 s2, v254, 33
	v_lshlrev_b32_e32 v67, 1, v67
	v_add_lshl_u32 v66, v66, s0, 1
	s_add_i32 s1, s2, s1
	v_add3_u32 v220, 0, v67, v66
	s_add_u32 s12, s22, 0x100000
	v_lshlrev_b64 v[66:67], 2, v[130:131]
	v_lshl_add_u32 v65, v65, 8, s1
	s_addc_u32 s13, s23, 0
	s_cmp_lt_u32 s4, 4
	s_cselect_b32 s40, s66, s94
	s_cselect_b32 s41, s67, s95
	s_and_b32 s1, s4, 3
	s_lshl_b32 s1, s1, 10
	s_add_u32 s40, s40, s1
	s_addc_u32 s41, s41, 0
	v_lshlrev_b32_e32 v74, 4, v128
	global_load_dwordx4 v[70:73], v74, s[40:41]
	s_lshl_b32 s1, s4, 10
	s_add_i32 s1, s1, 0x1a400
	v_add_u32_e32 v75, s1, v74
	v_add_u32_e32 v150, 0x1a400, v74
	s_lshl_b32 s1, s4, 1
	v_lshlrev_b64 v[66:67], 1, v[130:131]
	s_add_i32 s3, 0, 0x19200
	v_lshl_add_u64 v[154:155], s[14:15], 0, v[66:67]
	v_lshl_add_u64 v[66:67], s[22:23], 0, v[66:67]
	s_mov_b64 s[14:15], 0x2fc00000
	v_add_u32_e32 v223, s3, v130
	s_or_b32 s3, s1, 1
	v_lshl_add_u64 v[156:157], v[66:67], 0, s[14:15]
	v_lshl_add_u32 v66, v128, 3, 0
	s_mulk_i32 s3, 0x810
	v_readlane_b32 s14, v254, 34
	v_add_u32_e32 v224, s16, v66
	v_add_u32_e32 v225, s3, v66
	v_add_lshl_u32 v66, s0, v128, 2
	v_readlane_b32 s0, v254, 35
	v_add_u32_e32 v226, s14, v66
	v_lshlrev_b32_e32 v67, 3, v100
	v_add_u32_e32 v227, s0, v66
	v_add_u32_e32 v66, 0x100, v66
	v_add_u32_e32 v229, s0, v66
	v_readlane_b32 s0, v254, 14
	v_add_u32_e32 v221, s2, v67
	s_lshl_b32 s2, s4, 9
	s_add_i32 s16, s0, s1
	v_readlane_b32 s0, v254, 11
	v_sub_u32_e32 v160, 63, v128
	s_add_i32 s17, s0, s1
	v_readlane_b32 s0, v253, 29
	v_mov_b32_e32 v162, -1
	s_add_i32 s44, s2, 0
	v_lshl_add_u64 v[158:159], s[76:77], 0, v[130:131]
	v_add_u32_e32 v222, s14, v67
	v_add_u32_e32 v228, s14, v66
	s_waitcnt vmcnt(0)
	ds_write_b128 v75, v[70:73]
	v_mov_b32_e32 v149, v148
	v_mov_b32_e32 v129, v160
	s_add_i32 s18, s0, s1
	v_mov_b32_e32 v231, 0
	s_mov_b32 s19, 0
	v_add_u32_e32 v230, v65, v64
	s_add_i32 s44, s44, 0x19300
	s_mov_b32 s45, 0
	v_mov_b32_e32 v180, v162
	v_mov_b32_e32 v163, 0
	s_branch .Lln1_first

; __device__ __forceinline__ void phase_ln1(Frame& F0, const Args& A, int l, bool v_from_h) {
;     ...
;         tm_seg(F, 21);
;         {   LN1_GLDK(2); LN1_GLDK(3);
.Lln1_first:
	s_nop 4
	global_load_dwordx4 v[64:67], v219, s[20:21] offset:2048
	global_load_dwordx4 v[68:71], v219, s[24:25] offset:2048
	global_load_dwordx4 v[72:75], v219, s[26:27] offset:2048
	global_load_dwordx4 v[76:79], v219, s[42:43] offset:2048
	global_load_dwordx4 v[80:83], v219, s[50:51] offset:2048
	global_load_dwordx4 v[84:87], v219, s[62:63] offset:2048
	global_load_dwordx4 v[88:91], v219, s[68:69] offset:2048
	global_load_dwordx4 v[92:95], v219, s[74:75] offset:2048
	s_nop 4
	global_load_dwordx4 v[96:99], v219, s[20:21] offset:3072
	global_load_dwordx4 v[100:103], v219, s[24:25] offset:3072
	global_load_dwordx4 v[104:107], v219, s[26:27] offset:3072
	global_load_dwordx4 v[108:111], v219, s[42:43] offset:3072
	global_load_dwordx4 v[112:115], v219, s[50:51] offset:3072
	global_load_dwordx4 v[116:119], v219, s[62:63] offset:3072
	global_load_dwordx4 v[120:123], v219, s[68:69] offset:3072
	global_load_dwordx4 v[124:127], v219, s[74:75] offset:3072

; __device__ __forceinline__ void lds_barrier() { asm volatile("s_waitcnt lgkmcnt(0)" ::: "memory"); __builtin_amdgcn_s_barrier(); asm volatile("" ::: "memory"); }
; __device__ __forceinline__ void phase_ln1(Frame& F0, const Args& A, int l, bool v_from_h) {
;     ...
;         {   LN1_GLDK(2); LN1_GLDK(3);
;     ...
;         lds_barrier(); tm_seg(F, 23);
;         if (g + F.G < ngroups) { LN1_GLDK(0); LN1_GLDK(1); }
.LBB0_1296:
	s_waitcnt lgkmcnt(0)
	s_barrier
	s_andn2_b64 vcc, exec, s[14:15]
	s_cbranch_vccnz .LBB0_1298
	s_nop 4
	global_load_dwordx4 v[64:67], v219, s[20:21] offset:2048
	global_load_dwordx4 v[68:71], v219, s[24:25] offset:2048
	global_load_dwordx4 v[72:75], v219, s[26:27] offset:2048
	global_load_dwordx4 v[76:79], v219, s[42:43] offset:2048
	global_load_dwordx4 v[80:83], v219, s[50:51] offset:2048
	global_load_dwordx4 v[84:87], v219, s[62:63] offset:2048
	global_load_dwordx4 v[88:91], v219, s[68:69] offset:2048
	global_load_dwordx4 v[92:95], v219, s[74:75] offset:2048
	s_nop 4
	global_load_dwordx4 v[96:99], v219, s[20:21] offset:3072
	global_load_dwordx4 v[100:103], v219, s[24:25] offset:3072
	global_load_dwordx4 v[104:107], v219, s[26:27] offset:3072
	global_load_dwordx4 v[108:111], v219, s[42:43] offset:3072
	global_load_dwordx4 v[112:115], v219, s[50:51] offset:3072
	global_load_dwordx4 v[116:119], v219, s[62:63] offset:3072
	global_load_dwordx4 v[120:123], v219, s[68:69] offset:3072
	global_load_dwordx4 v[124:127], v219, s[74:75] offset:3072
